# P6 router top-4: branch-free compare/select butterfly (10 instr per step instead of ~21 with exec-masked moves), same comparisons and tie rule
# baseline (speedup 1.0000x reference)
.LBB0_975:
	v_mbcnt_lo_u32_b32 v129, -1, 0
	v_mbcnt_hi_u32_b32 v129, -1, v129
	s_nop 0
	v_and_b32_e32 v130, 15, v129
	v_lshrrev_b32_e32 v204, 3, v129
	v_lshl_add_u32 v205, v130, 13, s3
	v_bitop3_b32 v130, v204, v130, s42 bitop3:0x6c
	v_lshl_add_u32 v130, v130, 4, v205
	v_add_u32_e32 v206, 0, v130
	ds_read_b128 v[168:171], v206
	v_xad_u32 v172, v130, 16, 0
	ds_read_b128 v[172:175], v172
	s_waitcnt lgkmcnt(1)
	v_cvt_pk_bf16_f32 v176, v168, v169
	s_nop 0
	v_lshlrev_b32_e32 v177, 16, v176
	v_sub_f32_e32 v168, v168, v177
	v_and_b32_e32 v177, 0xffff0000, v176
	v_sub_f32_e32 v169, v169, v177
	v_cvt_pk_bf16_f32 v168, v168, v169
	v_cvt_pk_bf16_f32 v177, v170, v171
	s_nop 0
	v_lshlrev_b32_e32 v169, 16, v177
	v_sub_f32_e32 v169, v170, v169
	v_and_b32_e32 v170, 0xffff0000, v177
	v_sub_f32_e32 v170, v171, v170
	v_cvt_pk_bf16_f32 v169, v169, v170
	s_waitcnt lgkmcnt(0)
	v_cvt_pk_bf16_f32 v178, v172, v173
	s_nop 0
	v_lshlrev_b32_e32 v170, 16, v178
	v_and_b32_e32 v171, 0xffff0000, v178
	v_sub_f32_e32 v170, v172, v170
	v_sub_f32_e32 v171, v173, v171
	v_cvt_pk_bf16_f32 v170, v170, v171
	v_cvt_pk_bf16_f32 v179, v174, v175
	v_and_b32_e32 v171, 0xffffffe, v204
	v_mfma_f32_16x16x32_bf16 v[180:183], v[176:179], v[0:3], 0
	v_add_u32_e32 v171, 8, v171
	v_bitop3_b32 v129, v171, v129, 15 bitop3:0x78
	v_lshl_add_u32 v129, v129, 4, v205
	v_mfma_f32_16x16x32_bf16 v[200:203], v[176:179], v[8:11], 0
	v_lshlrev_b32_e32 v171, 16, v179
	v_sub_f32_e32 v171, v174, v171
	v_and_b32_e32 v172, 0xffff0000, v179
	v_mfma_f32_16x16x32_bf16 v[180:183], v[176:179], v[4:7], v[180:183]
	v_add_u32_e32 v204, 0, v129
	v_sub_f32_e32 v172, v175, v172
	v_cvt_pk_bf16_f32 v171, v171, v172
	v_mfma_f32_16x16x32_bf16 v[200:203], v[176:179], v[12:15], v[200:203]
	ds_read_b128 v[176:179], v204
	v_mfma_f32_16x16x32_bf16 v[172:175], v[168:171], v[0:3], v[180:183]
	s_nop 2
	v_xad_u32 v180, v129, 16, 0
	v_mfma_f32_16x16x32_bf16 v[168:171], v[168:171], v[8:11], v[200:203]
	ds_read_b128 v[180:183], v180
	s_waitcnt lgkmcnt(1)
	v_cvt_pk_bf16_f32 v200, v176, v177
	s_nop 0
	v_lshlrev_b32_e32 v201, 16, v200
	v_sub_f32_e32 v176, v176, v201
	v_and_b32_e32 v201, 0xffff0000, v200
	v_sub_f32_e32 v177, v177, v201
	v_cvt_pk_bf16_f32 v176, v176, v177
	v_cvt_pk_bf16_f32 v201, v178, v179
	s_nop 0
	v_lshlrev_b32_e32 v177, 16, v201
	v_sub_f32_e32 v177, v178, v177
	v_and_b32_e32 v178, 0xffff0000, v201
	v_sub_f32_e32 v178, v179, v178
	v_cvt_pk_bf16_f32 v177, v177, v178
	s_waitcnt lgkmcnt(0)
	v_cvt_pk_bf16_f32 v202, v180, v181
	s_nop 0
	v_lshlrev_b32_e32 v178, 16, v202
	v_sub_f32_e32 v178, v180, v178
	v_and_b32_e32 v179, 0xffff0000, v202
	v_sub_f32_e32 v179, v181, v179
	v_cvt_pk_bf16_f32 v178, v178, v179
	v_cvt_pk_bf16_f32 v203, v182, v183
	s_nop 0
	v_mfma_f32_16x16x32_bf16 v[172:175], v[200:203], v[16:19], v[172:175]
	v_lshlrev_b32_e32 v179, 16, v203
	v_and_b32_e32 v180, 0xffff0000, v203
	v_sub_f32_e32 v179, v182, v179
	v_mfma_f32_16x16x32_bf16 v[168:171], v[200:203], v[24:27], v[168:171]
	v_sub_f32_e32 v180, v183, v180
	v_cvt_pk_bf16_f32 v179, v179, v180
	ds_read_b128 v[180:183], v206 offset:256
	v_mfma_f32_16x16x32_bf16 v[172:175], v[200:203], v[20:23], v[172:175]
	v_mfma_f32_16x16x32_bf16 v[168:171], v[200:203], v[28:31], v[168:171]
	v_mfma_f32_16x16x32_bf16 v[172:175], v[176:179], v[16:19], v[172:175]
	v_mfma_f32_16x16x32_bf16 v[168:171], v[176:179], v[24:27], v[168:171]
	v_add_u32_e32 v176, 0x100, v130
	v_xad_u32 v176, v176, 16, 0
	ds_read_b128 v[176:179], v176
	s_waitcnt lgkmcnt(1)
	v_cvt_pk_bf16_f32 v200, v180, v181
	s_nop 0
	v_lshlrev_b32_e32 v201, 16, v200
	v_sub_f32_e32 v180, v180, v201
	v_and_b32_e32 v201, 0xffff0000, v200
	v_sub_f32_e32 v181, v181, v201
	v_cvt_pk_bf16_f32 v180, v180, v181
	v_cvt_pk_bf16_f32 v201, v182, v183
	s_nop 0
	v_lshlrev_b32_e32 v181, 16, v201
	v_sub_f32_e32 v181, v182, v181
	v_and_b32_e32 v182, 0xffff0000, v201
	v_sub_f32_e32 v182, v183, v182
	v_cvt_pk_bf16_f32 v181, v181, v182
	s_waitcnt lgkmcnt(0)
	v_cvt_pk_bf16_f32 v202, v176, v177
	s_nop 0
	v_lshlrev_b32_e32 v182, 16, v202
	v_sub_f32_e32 v176, v176, v182
	v_and_b32_e32 v182, 0xffff0000, v202
	v_sub_f32_e32 v177, v177, v182
	v_cvt_pk_bf16_f32 v182, v176, v177
	v_cvt_pk_bf16_f32 v203, v178, v179
	s_nop 0
	v_mfma_f32_16x16x32_bf16 v[172:175], v[200:203], v[32:35], v[172:175]
	v_lshlrev_b32_e32 v176, 16, v203
	v_and_b32_e32 v177, 0xffff0000, v203
	v_sub_f32_e32 v176, v178, v176
	v_mfma_f32_16x16x32_bf16 v[168:171], v[200:203], v[40:43], v[168:171]
	v_sub_f32_e32 v177, v179, v177
	v_cvt_pk_bf16_f32 v183, v176, v177
	ds_read_b128 v[176:179], v204 offset:256
	v_mfma_f32_16x16x32_bf16 v[172:175], v[200:203], v[36:39], v[172:175]
	v_mfma_f32_16x16x32_bf16 v[168:171], v[200:203], v[44:47], v[168:171]
	v_mfma_f32_16x16x32_bf16 v[172:175], v[180:183], v[32:35], v[172:175]
	v_mfma_f32_16x16x32_bf16 v[168:171], v[180:183], v[40:43], v[168:171]
	v_add_u32_e32 v180, 0x100, v129
	v_xad_u32 v180, v180, 16, 0
	ds_read_b128 v[180:183], v180
	s_waitcnt lgkmcnt(1)
	v_cvt_pk_bf16_f32 v200, v176, v177
	s_nop 0
	v_lshlrev_b32_e32 v201, 16, v200
	v_sub_f32_e32 v176, v176, v201
	v_and_b32_e32 v201, 0xffff0000, v200
	v_sub_f32_e32 v177, v177, v201
	v_cvt_pk_bf16_f32 v176, v176, v177
	v_cvt_pk_bf16_f32 v201, v178, v179
	s_nop 0
	v_lshlrev_b32_e32 v177, 16, v201
	v_sub_f32_e32 v177, v178, v177
	v_and_b32_e32 v178, 0xffff0000, v201
	v_sub_f32_e32 v178, v179, v178
	v_cvt_pk_bf16_f32 v177, v177, v178
	s_waitcnt lgkmcnt(0)
	v_cvt_pk_bf16_f32 v202, v180, v181
	s_nop 0
	v_lshlrev_b32_e32 v178, 16, v202
	v_sub_f32_e32 v178, v180, v178
	v_and_b32_e32 v179, 0xffff0000, v202
	v_sub_f32_e32 v179, v181, v179
	v_cvt_pk_bf16_f32 v178, v178, v179
	v_cvt_pk_bf16_f32 v203, v182, v183
	s_nop 0
	v_mfma_f32_16x16x32_bf16 v[172:175], v[200:203], v[48:51], v[172:175]
	v_lshlrev_b32_e32 v179, 16, v203
	v_and_b32_e32 v180, 0xffff0000, v203
	v_sub_f32_e32 v179, v182, v179
	v_mfma_f32_16x16x32_bf16 v[168:171], v[200:203], v[56:59], v[168:171]
	v_sub_f32_e32 v180, v183, v180
	v_cvt_pk_bf16_f32 v179, v179, v180
	ds_read_b128 v[180:183], v206 offset:512
	v_mfma_f32_16x16x32_bf16 v[172:175], v[200:203], v[52:55], v[172:175]
	v_mfma_f32_16x16x32_bf16 v[168:171], v[200:203], v[60:63], v[168:171]
	v_mfma_f32_16x16x32_bf16 v[172:175], v[176:179], v[48:51], v[172:175]
	v_mfma_f32_16x16x32_bf16 v[168:171], v[176:179], v[56:59], v[168:171]
	v_add_u32_e32 v176, 0x200, v130
	v_xad_u32 v176, v176, 16, 0
	ds_read_b128 v[176:179], v176
	s_waitcnt lgkmcnt(1)
	v_cvt_pk_bf16_f32 v200, v180, v181
	v_add_u32_e32 v130, 0x300, v130
	v_lshlrev_b32_e32 v201, 16, v200
	v_sub_f32_e32 v180, v180, v201
	v_and_b32_e32 v201, 0xffff0000, v200
	v_sub_f32_e32 v181, v181, v201
	v_cvt_pk_bf16_f32 v180, v180, v181
	v_cvt_pk_bf16_f32 v201, v182, v183
	v_xad_u32 v130, v130, 16, 0
	v_lshlrev_b32_e32 v181, 16, v201
	v_sub_f32_e32 v181, v182, v181
	v_and_b32_e32 v182, 0xffff0000, v201
	v_sub_f32_e32 v182, v183, v182
	v_cvt_pk_bf16_f32 v181, v181, v182
	s_waitcnt lgkmcnt(0)
	v_cvt_pk_bf16_f32 v202, v176, v177
	s_nop 0
	v_lshlrev_b32_e32 v182, 16, v202
	v_sub_f32_e32 v176, v176, v182
	v_and_b32_e32 v182, 0xffff0000, v202
	v_sub_f32_e32 v177, v177, v182
	v_cvt_pk_bf16_f32 v182, v176, v177
	v_cvt_pk_bf16_f32 v203, v178, v179
	s_nop 0
	v_mfma_f32_16x16x32_bf16 v[172:175], v[200:203], v[64:67], v[172:175]
	v_lshlrev_b32_e32 v176, 16, v203
	v_and_b32_e32 v177, 0xffff0000, v203
	v_sub_f32_e32 v176, v178, v176
	v_mfma_f32_16x16x32_bf16 v[168:171], v[200:203], v[72:75], v[168:171]
	v_sub_f32_e32 v177, v179, v177
	v_cvt_pk_bf16_f32 v183, v176, v177
	ds_read_b128 v[176:179], v204 offset:512
	v_mfma_f32_16x16x32_bf16 v[172:175], v[200:203], v[68:71], v[172:175]
	v_mfma_f32_16x16x32_bf16 v[168:171], v[200:203], v[76:79], v[168:171]
	v_mfma_f32_16x16x32_bf16 v[172:175], v[180:183], v[64:67], v[172:175]
	v_mfma_f32_16x16x32_bf16 v[168:171], v[180:183], v[72:75], v[168:171]
	v_add_u32_e32 v180, 0x200, v129
	v_xad_u32 v180, v180, 16, 0
	ds_read_b128 v[180:183], v180
	s_waitcnt lgkmcnt(1)
	v_cvt_pk_bf16_f32 v200, v176, v177
	v_add_u32_e32 v129, 0x300, v129
	v_lshlrev_b32_e32 v201, 16, v200
	v_sub_f32_e32 v176, v176, v201
	v_and_b32_e32 v201, 0xffff0000, v200
	v_sub_f32_e32 v177, v177, v201
	v_cvt_pk_bf16_f32 v176, v176, v177
	v_cvt_pk_bf16_f32 v201, v178, v179
	v_xad_u32 v129, v129, 16, 0
	v_lshlrev_b32_e32 v177, 16, v201
	v_sub_f32_e32 v177, v178, v177
	v_and_b32_e32 v178, 0xffff0000, v201
	v_sub_f32_e32 v178, v179, v178
	v_cvt_pk_bf16_f32 v177, v177, v178
	s_waitcnt lgkmcnt(0)
	v_cvt_pk_bf16_f32 v202, v180, v181
	s_nop 0
	v_lshlrev_b32_e32 v178, 16, v202
	v_sub_f32_e32 v178, v180, v178
	v_and_b32_e32 v179, 0xffff0000, v202
	v_sub_f32_e32 v179, v181, v179
	v_cvt_pk_bf16_f32 v178, v178, v179
	v_cvt_pk_bf16_f32 v203, v182, v183
	s_nop 0
	v_mfma_f32_16x16x32_bf16 v[172:175], v[200:203], v[80:83], v[172:175]
	v_lshlrev_b32_e32 v179, 16, v203
	v_and_b32_e32 v180, 0xffff0000, v203
	v_sub_f32_e32 v179, v182, v179
	v_mfma_f32_16x16x32_bf16 v[168:171], v[200:203], v[88:91], v[168:171]
	v_sub_f32_e32 v180, v183, v180
	v_cvt_pk_bf16_f32 v179, v179, v180
	ds_read_b128 v[180:183], v206 offset:768
	v_mfma_f32_16x16x32_bf16 v[172:175], v[200:203], v[84:87], v[172:175]
	v_mfma_f32_16x16x32_bf16 v[168:171], v[200:203], v[92:95], v[168:171]
	v_mfma_f32_16x16x32_bf16 v[172:175], v[176:179], v[80:83], v[172:175]
	v_mfma_f32_16x16x32_bf16 v[168:171], v[176:179], v[88:91], v[168:171]
	ds_read_b128 v[176:179], v130
	s_waitcnt lgkmcnt(1)
	v_cvt_pk_bf16_f32 v200, v180, v181
	s_nop 0
	v_lshlrev_b32_e32 v130, 16, v200
	v_sub_f32_e32 v130, v180, v130
	v_and_b32_e32 v180, 0xffff0000, v200
	v_sub_f32_e32 v180, v181, v180
	v_cvt_pk_bf16_f32 v180, v130, v180
	v_cvt_pk_bf16_f32 v201, v182, v183
	s_nop 0
	v_lshlrev_b32_e32 v130, 16, v201
	v_and_b32_e32 v181, 0xffff0000, v201
	v_sub_f32_e32 v130, v182, v130
	v_sub_f32_e32 v181, v183, v181
	v_cvt_pk_bf16_f32 v181, v130, v181
	s_waitcnt lgkmcnt(0)
	v_cvt_pk_bf16_f32 v202, v176, v177
	s_nop 0
	v_lshlrev_b32_e32 v130, 16, v202
	v_sub_f32_e32 v130, v176, v130
	v_and_b32_e32 v176, 0xffff0000, v202
	v_sub_f32_e32 v176, v177, v176
	v_cvt_pk_bf16_f32 v182, v130, v176
	v_cvt_pk_bf16_f32 v203, v178, v179
	s_nop 0
	v_mfma_f32_16x16x32_bf16 v[172:175], v[200:203], v[96:99], v[172:175]
	v_and_b32_e32 v176, 0xffff0000, v203
	v_lshlrev_b32_e32 v130, 16, v203
	v_sub_f32_e32 v176, v179, v176
	v_mfma_f32_16x16x32_bf16 v[168:171], v[200:203], v[104:107], v[168:171]
	v_sub_f32_e32 v130, v178, v130
	v_cvt_pk_bf16_f32 v183, v130, v176
	ds_read_b128 v[176:179], v204 offset:768
	v_mfma_f32_16x16x32_bf16 v[172:175], v[200:203], v[100:103], v[172:175]
	v_mfma_f32_16x16x32_bf16 v[168:171], v[200:203], v[108:111], v[168:171]
	v_mfma_f32_16x16x32_bf16 v[172:175], v[180:183], v[96:99], v[172:175]
	v_mfma_f32_16x16x32_bf16 v[168:171], v[180:183], v[104:107], v[168:171]
	ds_read_b128 v[180:183], v129
	s_waitcnt lgkmcnt(1)
	v_cvt_pk_bf16_f32 v200, v176, v177
	s_nop 0
	v_lshlrev_b32_e32 v129, 16, v200
	v_and_b32_e32 v130, 0xffff0000, v200
	v_sub_f32_e32 v129, v176, v129
	v_sub_f32_e32 v130, v177, v130
	v_cvt_pk_bf16_f32 v176, v129, v130
	v_cvt_pk_bf16_f32 v201, v178, v179
	s_nop 0
	v_lshlrev_b32_e32 v129, 16, v201
	v_and_b32_e32 v130, 0xffff0000, v201
	v_sub_f32_e32 v129, v178, v129
	v_sub_f32_e32 v130, v179, v130
	v_cvt_pk_bf16_f32 v177, v129, v130
	s_waitcnt lgkmcnt(0)
	v_cvt_pk_bf16_f32 v202, v180, v181
	s_nop 0
	v_lshlrev_b32_e32 v129, 16, v202
	v_and_b32_e32 v130, 0xffff0000, v202
	v_sub_f32_e32 v129, v180, v129
	v_sub_f32_e32 v130, v181, v130
	v_cvt_pk_bf16_f32 v178, v129, v130
	v_cvt_pk_bf16_f32 v203, v182, v183
	s_nop 0
	v_mfma_f32_16x16x32_bf16 v[172:175], v[200:203], v[112:115], v[172:175]
	v_lshlrev_b32_e32 v129, 16, v203
	v_and_b32_e32 v130, 0xffff0000, v203
	v_sub_f32_e32 v129, v182, v129
	v_mfma_f32_16x16x32_bf16 v[168:171], v[200:203], v[120:123], v[168:171]
	v_sub_f32_e32 v130, v183, v130
	v_cvt_pk_bf16_f32 v179, v129, v130
	v_mfma_f32_16x16x32_bf16 v[172:175], v[200:203], v[116:119], v[172:175]
	v_mfma_f32_16x16x32_bf16 v[168:171], v[200:203], v[124:127], v[168:171]
	v_mfma_f32_16x16x32_bf16 v[172:175], v[176:179], v[112:115], v[172:175]
	v_mfma_f32_16x16x32_bf16 v[168:171], v[176:179], v[120:123], v[168:171]
	s_nop 7
	ds_write2_b32 v197, v172, v168 offset1:16
	ds_write2_b32 v197, v173, v169 offset0:32 offset1:48
	ds_write2_b32 v197, v174, v170 offset0:64 offset1:80
	ds_write2_b32 v197, v175, v171 offset0:96 offset1:112
	s_waitcnt lgkmcnt(0)
	s_barrier
	v_mov_b32_e32 v129, v246
	ds_read2st64_b32 v[168:169], v191 offset1:8
	ds_read2st64_b32 v[170:171], v191 offset0:16 offset1:24
	ds_read2st64_b32 v[172:173], v191 offset0:32 offset1:40
	s_waitcnt lgkmcnt(2)
	v_add_f32_e32 v129, v129, v168
	v_add_f32_e32 v129, v129, v169
	ds_read2st64_b32 v[168:169], v191 offset0:48 offset1:56
	s_waitcnt lgkmcnt(2)
	v_add_f32_e32 v129, v129, v170
	v_add_f32_e32 v129, v129, v171
	s_waitcnt lgkmcnt(1)
	v_add_f32_e32 v129, v129, v172
	v_add_f32_e32 v129, v129, v173
	s_waitcnt lgkmcnt(0)
	v_add_f32_e32 v129, v129, v168
	v_add_f32_e32 v168, v129, v169
	v_mov_b32_e32 v247, v168
	v_mov_b32_e32 v248, v247
	v_mov_b32_e32 v249, v190
	s_nop 0
	v_mov_b32_dpp v250, v248 quad_perm:[1,0,3,2] row_mask:0xf bank_mask:0xf
	v_mov_b32_dpp v251, v249 quad_perm:[1,0,3,2] row_mask:0xf bank_mask:0xf
	v_cmp_gt_f32_e32 vcc, v250, v248
	v_cmp_eq_f32_e64 s[12:13], v250, v248
	v_cmp_lt_i32_e64 s[14:15], v251, v249
	s_and_b64 s[12:13], s[12:13], s[14:15]
	s_or_b64 s[12:13], vcc, s[12:13]
	v_cndmask_b32_e64 v248, v248, v250, s[12:13]
	v_cndmask_b32_e64 v249, v249, v251, s[12:13]
	s_nop 0
	v_mov_b32_dpp v250, v248 quad_perm:[2,3,0,1] row_mask:0xf bank_mask:0xf
	v_mov_b32_dpp v251, v249 quad_perm:[2,3,0,1] row_mask:0xf bank_mask:0xf
	v_cmp_gt_f32_e32 vcc, v250, v248
	v_cmp_eq_f32_e64 s[12:13], v250, v248
	v_cmp_lt_i32_e64 s[14:15], v251, v249
	s_and_b64 s[12:13], s[12:13], s[14:15]
	s_or_b64 s[12:13], vcc, s[12:13]
	v_cndmask_b32_e64 v248, v248, v250, s[12:13]
	v_cndmask_b32_e64 v249, v249, v251, s[12:13]
	s_nop 0
	v_mov_b32_dpp v250, v248 row_half_mirror row_mask:0xf bank_mask:0xf
	v_mov_b32_dpp v251, v249 row_half_mirror row_mask:0xf bank_mask:0xf
	v_cmp_gt_f32_e32 vcc, v250, v248
	v_cmp_eq_f32_e64 s[12:13], v250, v248
	v_cmp_lt_i32_e64 s[14:15], v251, v249
	s_and_b64 s[12:13], s[12:13], s[14:15]
	s_or_b64 s[12:13], vcc, s[12:13]
	v_cndmask_b32_e64 v248, v248, v250, s[12:13]
	v_cndmask_b32_e64 v249, v249, v251, s[12:13]
	s_nop 0
	v_mov_b32_dpp v250, v248 row_mirror row_mask:0xf bank_mask:0xf
	v_mov_b32_dpp v251, v249 row_mirror row_mask:0xf bank_mask:0xf
	v_cmp_gt_f32_e32 vcc, v250, v248
	v_cmp_eq_f32_e64 s[12:13], v250, v248
	v_cmp_lt_i32_e64 s[14:15], v251, v249
	s_and_b64 s[12:13], s[12:13], s[14:15]
	s_or_b64 s[12:13], vcc, s[12:13]
	v_cndmask_b32_e64 v248, v248, v250, s[12:13]
	v_cndmask_b32_e64 v249, v249, v251, s[12:13]
	ds_swizzle_b32 v250, v248 offset:swizzle(SWAP,16)
	ds_swizzle_b32 v251, v249 offset:swizzle(SWAP,16)
	s_waitcnt lgkmcnt(0)
	v_cmp_gt_f32_e32 vcc, v250, v248
	v_cmp_eq_f32_e64 s[12:13], v250, v248
	v_cmp_lt_i32_e64 s[14:15], v251, v249
	s_and_b64 s[12:13], s[12:13], s[14:15]
	s_or_b64 s[12:13], vcc, s[12:13]
	v_cndmask_b32_e64 v248, v248, v250, s[12:13]
	v_cndmask_b32_e64 v249, v249, v251, s[12:13]
	v_cmp_eq_u32_e32 vcc, v249, v190
	v_mov_b32_e32 v130, v248
	v_mov_b32_e32 v129, v249
	v_cndmask_b32_e32 v247, v247, v199, vcc
	v_mov_b32_e32 v248, v247
	v_mov_b32_e32 v249, v190
	s_nop 0
	v_mov_b32_dpp v250, v248 quad_perm:[1,0,3,2] row_mask:0xf bank_mask:0xf
	v_mov_b32_dpp v251, v249 quad_perm:[1,0,3,2] row_mask:0xf bank_mask:0xf
	v_cmp_gt_f32_e32 vcc, v250, v248
	v_cmp_eq_f32_e64 s[12:13], v250, v248
	v_cmp_lt_i32_e64 s[14:15], v251, v249
	s_and_b64 s[12:13], s[12:13], s[14:15]
	s_or_b64 s[12:13], vcc, s[12:13]
	v_cndmask_b32_e64 v248, v248, v250, s[12:13]
	v_cndmask_b32_e64 v249, v249, v251, s[12:13]
	s_nop 0
	v_mov_b32_dpp v250, v248 quad_perm:[2,3,0,1] row_mask:0xf bank_mask:0xf
	v_mov_b32_dpp v251, v249 quad_perm:[2,3,0,1] row_mask:0xf bank_mask:0xf
	v_cmp_gt_f32_e32 vcc, v250, v248
	v_cmp_eq_f32_e64 s[12:13], v250, v248
	v_cmp_lt_i32_e64 s[14:15], v251, v249
	s_and_b64 s[12:13], s[12:13], s[14:15]
	s_or_b64 s[12:13], vcc, s[12:13]
	v_cndmask_b32_e64 v248, v248, v250, s[12:13]
	v_cndmask_b32_e64 v249, v249, v251, s[12:13]
	s_nop 0
	v_mov_b32_dpp v250, v248 row_half_mirror row_mask:0xf bank_mask:0xf
	v_mov_b32_dpp v251, v249 row_half_mirror row_mask:0xf bank_mask:0xf
	v_cmp_gt_f32_e32 vcc, v250, v248
	v_cmp_eq_f32_e64 s[12:13], v250, v248
	v_cmp_lt_i32_e64 s[14:15], v251, v249
	s_and_b64 s[12:13], s[12:13], s[14:15]
	s_or_b64 s[12:13], vcc, s[12:13]
	v_cndmask_b32_e64 v248, v248, v250, s[12:13]
	v_cndmask_b32_e64 v249, v249, v251, s[12:13]
	s_nop 0
	v_mov_b32_dpp v250, v248 row_mirror row_mask:0xf bank_mask:0xf
	v_mov_b32_dpp v251, v249 row_mirror row_mask:0xf bank_mask:0xf
	v_cmp_gt_f32_e32 vcc, v250, v248
	v_cmp_eq_f32_e64 s[12:13], v250, v248
	v_cmp_lt_i32_e64 s[14:15], v251, v249
	s_and_b64 s[12:13], s[12:13], s[14:15]
	s_or_b64 s[12:13], vcc, s[12:13]
	v_cndmask_b32_e64 v248, v248, v250, s[12:13]
	v_cndmask_b32_e64 v249, v249, v251, s[12:13]
	ds_swizzle_b32 v250, v248 offset:swizzle(SWAP,16)
	ds_swizzle_b32 v251, v249 offset:swizzle(SWAP,16)
	s_waitcnt lgkmcnt(0)
	v_cmp_gt_f32_e32 vcc, v250, v248
	v_cmp_eq_f32_e64 s[12:13], v250, v248
	v_cmp_lt_i32_e64 s[14:15], v251, v249
	s_and_b64 s[12:13], s[12:13], s[14:15]
	s_or_b64 s[12:13], vcc, s[12:13]
	v_cndmask_b32_e64 v248, v248, v250, s[12:13]
	v_cndmask_b32_e64 v249, v249, v251, s[12:13]
	v_cmp_eq_u32_e32 vcc, v249, v190
	v_mov_b32_e32 v170, v248
	v_mov_b32_e32 v169, v249
	v_cndmask_b32_e32 v247, v247, v199, vcc
	v_mov_b32_e32 v248, v247
	v_mov_b32_e32 v249, v190
	s_nop 0
	v_mov_b32_dpp v250, v248 quad_perm:[1,0,3,2] row_mask:0xf bank_mask:0xf
	v_mov_b32_dpp v251, v249 quad_perm:[1,0,3,2] row_mask:0xf bank_mask:0xf
	v_cmp_gt_f32_e32 vcc, v250, v248
	v_cmp_eq_f32_e64 s[12:13], v250, v248
	v_cmp_lt_i32_e64 s[14:15], v251, v249
	s_and_b64 s[12:13], s[12:13], s[14:15]
	s_or_b64 s[12:13], vcc, s[12:13]
	v_cndmask_b32_e64 v248, v248, v250, s[12:13]
	v_cndmask_b32_e64 v249, v249, v251, s[12:13]
	s_nop 0
	v_mov_b32_dpp v250, v248 quad_perm:[2,3,0,1] row_mask:0xf bank_mask:0xf
	v_mov_b32_dpp v251, v249 quad_perm:[2,3,0,1] row_mask:0xf bank_mask:0xf
	v_cmp_gt_f32_e32 vcc, v250, v248
	v_cmp_eq_f32_e64 s[12:13], v250, v248
	v_cmp_lt_i32_e64 s[14:15], v251, v249
	s_and_b64 s[12:13], s[12:13], s[14:15]
	s_or_b64 s[12:13], vcc, s[12:13]
	v_cndmask_b32_e64 v248, v248, v250, s[12:13]
	v_cndmask_b32_e64 v249, v249, v251, s[12:13]
	s_nop 0
	v_mov_b32_dpp v250, v248 row_half_mirror row_mask:0xf bank_mask:0xf
	v_mov_b32_dpp v251, v249 row_half_mirror row_mask:0xf bank_mask:0xf
	v_cmp_gt_f32_e32 vcc, v250, v248
	v_cmp_eq_f32_e64 s[12:13], v250, v248
	v_cmp_lt_i32_e64 s[14:15], v251, v249
	s_and_b64 s[12:13], s[12:13], s[14:15]
	s_or_b64 s[12:13], vcc, s[12:13]
	v_cndmask_b32_e64 v248, v248, v250, s[12:13]
	v_cndmask_b32_e64 v249, v249, v251, s[12:13]
	s_nop 0
	v_mov_b32_dpp v250, v248 row_mirror row_mask:0xf bank_mask:0xf
	v_mov_b32_dpp v251, v249 row_mirror row_mask:0xf bank_mask:0xf
	v_cmp_gt_f32_e32 vcc, v250, v248
	v_cmp_eq_f32_e64 s[12:13], v250, v248
	v_cmp_lt_i32_e64 s[14:15], v251, v249
	s_and_b64 s[12:13], s[12:13], s[14:15]
	s_or_b64 s[12:13], vcc, s[12:13]
	v_cndmask_b32_e64 v248, v248, v250, s[12:13]
	v_cndmask_b32_e64 v249, v249, v251, s[12:13]
	ds_swizzle_b32 v250, v248 offset:swizzle(SWAP,16)
	ds_swizzle_b32 v251, v249 offset:swizzle(SWAP,16)
	s_waitcnt lgkmcnt(0)
	v_cmp_gt_f32_e32 vcc, v250, v248
	v_cmp_eq_f32_e64 s[12:13], v250, v248
	v_cmp_lt_i32_e64 s[14:15], v251, v249
	s_and_b64 s[12:13], s[12:13], s[14:15]
	s_or_b64 s[12:13], vcc, s[12:13]
	v_cndmask_b32_e64 v248, v248, v250, s[12:13]
	v_cndmask_b32_e64 v249, v249, v251, s[12:13]
	v_cmp_eq_u32_e32 vcc, v249, v190
	v_mov_b32_e32 v171, v248
	v_mov_b32_e32 v172, v249
	v_cndmask_b32_e32 v247, v247, v199, vcc
	v_mov_b32_e32 v248, v247
	v_mov_b32_e32 v249, v190
	s_nop 0
	v_mov_b32_dpp v250, v248 quad_perm:[1,0,3,2] row_mask:0xf bank_mask:0xf
	v_mov_b32_dpp v251, v249 quad_perm:[1,0,3,2] row_mask:0xf bank_mask:0xf
	v_cmp_gt_f32_e32 vcc, v250, v248
	v_cmp_eq_f32_e64 s[12:13], v250, v248
	v_cmp_lt_i32_e64 s[14:15], v251, v249
	s_and_b64 s[12:13], s[12:13], s[14:15]
	s_or_b64 s[12:13], vcc, s[12:13]
	v_cndmask_b32_e64 v248, v248, v250, s[12:13]
	v_cndmask_b32_e64 v249, v249, v251, s[12:13]
	s_nop 0
	v_mov_b32_dpp v250, v248 quad_perm:[2,3,0,1] row_mask:0xf bank_mask:0xf
	v_mov_b32_dpp v251, v249 quad_perm:[2,3,0,1] row_mask:0xf bank_mask:0xf
	v_cmp_gt_f32_e32 vcc, v250, v248
	v_cmp_eq_f32_e64 s[12:13], v250, v248
	v_cmp_lt_i32_e64 s[14:15], v251, v249
	s_and_b64 s[12:13], s[12:13], s[14:15]
	s_or_b64 s[12:13], vcc, s[12:13]
	v_cndmask_b32_e64 v248, v248, v250, s[12:13]
	v_cndmask_b32_e64 v249, v249, v251, s[12:13]
	s_nop 0
	v_mov_b32_dpp v250, v248 row_half_mirror row_mask:0xf bank_mask:0xf
	v_mov_b32_dpp v251, v249 row_half_mirror row_mask:0xf bank_mask:0xf
	v_cmp_gt_f32_e32 vcc, v250, v248
	v_cmp_eq_f32_e64 s[12:13], v250, v248
	v_cmp_lt_i32_e64 s[14:15], v251, v249
	s_and_b64 s[12:13], s[12:13], s[14:15]
	s_or_b64 s[12:13], vcc, s[12:13]
	v_cndmask_b32_e64 v248, v248, v250, s[12:13]
	v_cndmask_b32_e64 v249, v249, v251, s[12:13]
	s_nop 0
	v_mov_b32_dpp v250, v248 row_mirror row_mask:0xf bank_mask:0xf
	v_mov_b32_dpp v251, v249 row_mirror row_mask:0xf bank_mask:0xf
	v_cmp_gt_f32_e32 vcc, v250, v248
	v_cmp_eq_f32_e64 s[12:13], v250, v248
	v_cmp_lt_i32_e64 s[14:15], v251, v249
	s_and_b64 s[12:13], s[12:13], s[14:15]
	s_or_b64 s[12:13], vcc, s[12:13]
	v_cndmask_b32_e64 v248, v248, v250, s[12:13]
	v_cndmask_b32_e64 v249, v249, v251, s[12:13]
	ds_swizzle_b32 v250, v248 offset:swizzle(SWAP,16)
	ds_swizzle_b32 v251, v249 offset:swizzle(SWAP,16)
	s_waitcnt lgkmcnt(0)
	v_cmp_gt_f32_e32 vcc, v250, v248
	v_cmp_eq_f32_e64 s[12:13], v250, v248
	v_cmp_lt_i32_e64 s[14:15], v251, v249
	s_and_b64 s[12:13], s[12:13], s[14:15]
	s_or_b64 s[12:13], vcc, s[12:13]
	v_cndmask_b32_e64 v248, v248, v250, s[12:13]
	v_cndmask_b32_e64 v249, v249, v251, s[12:13]
	v_mov_b32_e32 v168, v248
	v_mov_b32_e32 v173, v249
	s_and_saveexec_b64 s[12:13], s[4:5]
	s_cbranch_execnz .LBB0_1057
.LBB0_1054:
	s_or_b64 exec, exec, s[12:13]
	s_add_i32 s25, s25, 1
	s_cmp_lg_u32 s25, 8
	s_cbranch_scc1 .LBB0_972
	s_branch .LBB0_1058
.LBB0_1057:
	v_sub_f32_e32 v170, v170, v130
	v_mul_f32_e32 v170, 0x3fb8aa3b, v170
	v_sub_f32_e32 v171, v171, v130
	v_exp_f32_e32 v170, v170
	v_mul_f32_e32 v171, 0x3fb8aa3b, v171
	v_sub_f32_e32 v130, v168, v130
	v_exp_f32_e32 v171, v171
	v_mul_f32_e32 v130, 0x3fb8aa3b, v130
	v_exp_f32_e32 v130, v130
	v_add_f32_e32 v168, 1.0, v170
	v_add_f32_e32 v168, v168, v171
	v_add_f32_e32 v168, v168, v130
	v_div_scale_f32 v174, s[14:15], v168, v168, 1.0
	s_waitcnt lgkmcnt(0)
	v_rcp_f32_e32 v175, v174
	v_cndmask_b32_e64 v130, v130, v171, s[10:11]
	v_cndmask_b32_e64 v130, v130, v170, s[8:9]
	v_cndmask_b32_e64 v130, v130, 1.0, s[6:7]
	v_fma_f32 v176, -v174, v175, 1.0
	v_fmac_f32_e32 v175, v176, v175
	v_div_scale_f32 v176, vcc, 1.0, v168, 1.0
	v_mul_f32_e32 v177, v176, v175
	v_fma_f32 v178, -v174, v177, v176
	v_fmac_f32_e32 v177, v178, v175
	v_fma_f32 v174, -v174, v177, v176
	v_div_fmas_f32 v174, v174, v175, v177
	v_div_fixup_f32 v168, v174, v168, 1.0
	v_mul_f32_e32 v130, v168, v130
	v_cndmask_b32_e64 v168, v173, v172, s[10:11]
	v_cndmask_b32_e64 v168, v168, v169, s[8:9]
	v_cndmask_b32_e64 v129, v168, v129, s[6:7]
	v_lshl_add_u32 v168, s25, 10, v192
	ds_write_b96 v168, v[128:130]
	s_or_b64 exec, exec, s[12:13]
	s_add_i32 s25, s25, 1
	s_cmp_lg_u32 s25, 8
	s_cbranch_scc1 .LBB0_972
